# attention: half-wave stagger - waves 0-3 run the plain tile loop, waves 4-7 the rotated one (last PV block after the tile barrier), so SIMD partners are out of lockstep; barrier protocol unchanged
# speedup vs baseline: 1.0041x; 1.0026x over previous
.LBB0_438:
	s_lshl_b32 s2, s12, 1
	s_and_b32 s2, s2, 14
	s_ashr_i32 s3, s12, 7
	s_add_i32 s2, s2, s3
	s_ashr_i32 s3, s2, 2
	s_lshl_b32 s22, s3, 8
	s_lshl_b32 s21, s3, 12
	s_lshl_b32 s3, s12, 5
	s_lshl_b32 s2, s2, 7
	v_mov_b32_e32 v205, v3
	v_readlane_b32 s8, v254, 27
	s_and_b32 s3, s3, 0xf00
	s_and_b32 s10, s2, 0x180
	v_mbcnt_lo_u32_b32 v0, -1, 0
	v_mbcnt_hi_u32_b32 v0, -1, v0
	s_add_i32 s13, s22, 0x4000
	v_add_u32_e32 v204, s8, v0
	s_or_b32 s11, s21, s3
	s_lshl_b32 s80, s10, 1
	s_add_u32 s2, s52, s80
	v_lshlrev_b32_e32 v0, 4, v204
	v_add_u32_e32 v6, 0x200, v204
	v_add_u32_e32 v12, 0x400, v204
	v_add_u32_e32 v14, 0x600, v204
	s_addc_u32 s3, s53, 0
	v_and_b32_e32 v2, 0xf0, v0
	v_ashrrev_i32_e32 v36, 4, v204
	v_ashrrev_i32_e32 v38, 4, v6
	v_ashrrev_i32_e32 v40, 4, v12
	v_ashrrev_i32_e32 v42, 4, v14
	v_add_u32_e32 v20, 0x800, v204
	v_add_u32_e32 v22, 0xa00, v204
	v_lshl_add_u64 v[0:1], s[2:3], 0, v[2:3]
	v_add_u32_e32 v4, s11, v36
	s_movk_i32 s18, 0x1400
	v_add_u32_e32 v6, s11, v38
	v_add_u32_e32 v12, s11, v40
	v_add_u32_e32 v14, s11, v42
	v_ashrrev_i32_e32 v44, 4, v20
	v_ashrrev_i32_e32 v46, 4, v22
	v_add_u32_e32 v28, 0xc00, v204
	v_add_u32_e32 v32, 0xe00, v204
	v_mad_i64_i32 v[4:5], s[8:9], v4, s18, v[0:1]
	v_mad_i64_i32 v[8:9], s[8:9], v6, s18, v[0:1]
	v_mad_i64_i32 v[12:13], s[8:9], v12, s18, v[0:1]
	v_mad_i64_i32 v[16:17], s[8:9], v14, s18, v[0:1]
	v_add_u32_e32 v20, s11, v44
	v_add_u32_e32 v22, s11, v46
	v_ashrrev_i32_e32 v47, 4, v28
	v_ashrrev_i32_e32 v48, 4, v32
	global_load_dwordx4 v[4:7], v[4:5], off
	s_nop 0
	global_load_dwordx4 v[8:11], v[8:9], off
	s_nop 0
	global_load_dwordx4 v[12:15], v[12:13], off
	s_nop 0
	global_load_dwordx4 v[16:19], v[16:17], off
	v_mad_i64_i32 v[20:21], s[8:9], v20, s18, v[0:1]
	v_mad_i64_i32 v[24:25], s[8:9], v22, s18, v[0:1]
	v_add_u32_e32 v28, s11, v47
	v_add_u32_e32 v32, s11, v48
	global_load_dwordx4 v[20:23], v[20:21], off
	s_nop 0
	global_load_dwordx4 v[24:27], v[24:25], off
	v_mad_i64_i32 v[28:29], s[8:9], v28, s18, v[0:1]
	v_mad_i64_i32 v[0:1], s[8:9], v32, s18, v[0:1]
	global_load_dwordx4 v[28:31], v[28:29], off
	v_add_u32_e32 v206, 0x11800, v205
	global_load_dwordx4 v[32:35], v[0:1], off
	v_add_u32_e32 v0, v206, v2
	v_mad_u64_u32 v[36:37], s[14:15], v36, s30, v[0:1]
	v_mad_u64_u32 v[38:39], s[14:15], v38, s30, v[0:1]
	v_mad_u64_u32 v[40:41], s[14:15], v40, s30, v[0:1]
	v_mad_u64_u32 v[42:43], s[14:15], v42, s30, v[0:1]
	v_mad_u64_u32 v[44:45], s[14:15], v44, s30, v[0:1]
	v_and_b32_e32 v2, 63, v204
	v_ashrrev_i32_e32 v49, 6, v204
	s_mov_b64 s[24:25], 0x400
	v_readfirstlane_b32 s8, v49
	s_mov_b32 s23, 0
	v_mov_b32_e32 v210, 0
	v_mov_b32_e32 v208, 0xf149f2ca
	v_mov_b32_e32 v209, 0xf149f2ca
	v_mov_b32_e32 v207, 0
	s_waitcnt vmcnt(7)
	ds_write_b128 v36, v[4:7]
	s_waitcnt vmcnt(6)
	ds_write_b128 v38, v[8:11]
	s_waitcnt vmcnt(5)
	ds_write_b128 v40, v[12:15]
	s_waitcnt vmcnt(4)
	ds_write_b128 v42, v[16:19]
	s_waitcnt vmcnt(3)
	ds_write_b128 v44, v[20:23]
	v_mad_u64_u32 v[4:5], s[14:15], v46, s30, v[0:1]
	s_waitcnt vmcnt(2)
	ds_write_b128 v4, v[24:27]
	v_mad_u64_u32 v[4:5], s[14:15], v47, s30, v[0:1]
	v_mad_u64_u32 v[0:1], s[14:15], v48, s30, v[0:1]
	s_waitcnt vmcnt(1)
	ds_write_b128 v4, v[28:31]
	s_waitcnt vmcnt(0)
	ds_write_b128 v0, v[32:35]
	v_or_b32_e32 v4, s13, v2
	v_mov_b64_e32 v[0:1], s[52:53]
	v_mad_i64_i32 v[0:1], s[14:15], v4, s18, v[0:1]
	s_lshl_b32 s14, s8, 3
	s_add_i32 s15, s21, 0xffffff00
	s_cmp_lt_i32 s8, 32
	s_cselect_b32 s9, s13, s15
	s_add_i32 s9, s9, s14
	s_mul_hi_i32 s18, s9, 0x1400
	s_mulk_i32 s9, 0x1400
	s_add_u32 s9, s52, s9
	v_lshlrev_b32_e32 v4, 3, v49
	s_addc_u32 s19, s53, s18
	v_lshl_add_u64 v[0:1], v[0:1], 0, s[80:81]
	v_ashrrev_i32_e32 v5, 31, v4
	s_add_u32 s18, s9, s80
	v_lshl_add_u64 v[0:1], v[4:5], 1, v[0:1]
	s_addc_u32 s19, s19, 0
	v_lshlrev_b32_e32 v2, 2, v2
	global_load_dwordx4 v[176:179], v[0:1], off offset:2048
	global_load_dwordx4 v[180:183], v[0:1], off offset:2176
	v_lshl_add_u64 v[0:1], s[18:19], 0, v[2:3]
	s_mul_i32 s19, s8, 0x880
	v_add_u32_e32 v4, s19, v205
	s_or_b32 s20, s14, 1
	v_readfirstlane_b32 s9, v4
	s_cmpk_lt_i32 s20, 0x100
	s_mov_b32 m0, s9
	s_cselect_b32 s9, s13, s15
	s_add_i32 s9, s9, s20
	s_mul_hi_i32 s18, s9, 0x1400
	s_mulk_i32 s9, 0x1400
	s_add_u32 s9, s52, s9
	s_mulk_i32 s20, 0x110
	s_addc_u32 s18, s53, s18
	v_add_u32_e32 v4, s20, v205
	v_lshl_add_u64 v[0:1], v[0:1], 0, s[24:25]
	s_add_u32 s26, s9, s80
	v_readfirstlane_b32 s9, v4
	global_load_lds_dword v[0:1], off
	s_addc_u32 s27, s18, 0
	s_mov_b32 m0, s9
	s_or_b32 s9, s14, 2
	s_cmpk_lt_i32 s9, 0x100
	s_cselect_b32 s18, s13, s15
	s_add_i32 s9, s18, s9
	s_mul_hi_i32 s18, s9, 0x1400
	s_mulk_i32 s9, 0x1400
	s_add_u32 s9, s52, s9
	s_addc_u32 s18, s53, s18
	v_lshl_add_u64 v[0:1], s[26:27], 0, v[2:3]
	s_add_u32 s26, s9, s80
	s_addc_u32 s27, s18, 0
	s_add_i32 s9, s20, 0x110
	v_add_u32_e32 v4, s9, v205
	v_lshl_add_u64 v[0:1], v[0:1], 0, s[24:25]
	v_readfirstlane_b32 s9, v4
	global_load_lds_dword v[0:1], off
	s_mov_b32 m0, s9
	s_or_b32 s9, s14, 3
	s_cmpk_lt_i32 s9, 0x100
	s_cselect_b32 s18, s13, s15
	s_add_i32 s9, s18, s9
	s_mul_hi_i32 s18, s9, 0x1400
	s_mulk_i32 s9, 0x1400
	s_add_u32 s9, s52, s9
	s_addc_u32 s18, s53, s18
	v_lshl_add_u64 v[0:1], s[26:27], 0, v[2:3]
	s_add_u32 s26, s9, s80
	s_addc_u32 s27, s18, 0
	s_add_i32 s9, s20, 0x220
	v_add_u32_e32 v4, s9, v205
	v_lshl_add_u64 v[0:1], v[0:1], 0, s[24:25]
	v_readfirstlane_b32 s9, v4
	global_load_lds_dword v[0:1], off
	s_mov_b32 m0, s9
	s_or_b32 s9, s14, 4
	s_cmpk_lt_i32 s9, 0x100
	s_cselect_b32 s18, s13, s15
	s_add_i32 s9, s18, s9
	s_mul_hi_i32 s18, s9, 0x1400
	s_mulk_i32 s9, 0x1400
	s_add_u32 s9, s52, s9
	s_addc_u32 s18, s53, s18
	v_lshl_add_u64 v[0:1], s[26:27], 0, v[2:3]
	s_add_u32 s26, s9, s80
	s_addc_u32 s27, s18, 0
	s_add_i32 s9, s20, 0x330
	v_add_u32_e32 v4, s9, v205
	v_lshl_add_u64 v[0:1], v[0:1], 0, s[24:25]
	v_readfirstlane_b32 s9, v4
	global_load_lds_dword v[0:1], off
	s_mov_b32 m0, s9
	s_or_b32 s9, s14, 5
	s_cmpk_lt_i32 s9, 0x100
	s_cselect_b32 s18, s13, s15
	s_add_i32 s9, s18, s9
	s_mul_hi_i32 s18, s9, 0x1400
	s_mulk_i32 s9, 0x1400
	s_add_u32 s9, s52, s9
	s_addc_u32 s18, s53, s18
	v_lshl_add_u64 v[0:1], s[26:27], 0, v[2:3]
	s_add_u32 s26, s9, s80
	s_addc_u32 s27, s18, 0
	s_add_i32 s9, s20, 0x440
	v_add_u32_e32 v4, s9, v205
	v_lshl_add_u64 v[0:1], v[0:1], 0, s[24:25]
	v_readfirstlane_b32 s9, v4
	global_load_lds_dword v[0:1], off
	s_mov_b32 m0, s9
	s_or_b32 s9, s14, 6
	s_cmpk_lt_i32 s9, 0x100
	s_cselect_b32 s18, s13, s15
	s_add_i32 s9, s18, s9
	s_mul_hi_i32 s18, s9, 0x1400
	s_mulk_i32 s9, 0x1400
	s_add_u32 s9, s52, s9
	s_addc_u32 s18, s53, s18
	v_lshl_add_u64 v[0:1], s[26:27], 0, v[2:3]
	s_add_u32 s26, s9, s80
	s_addc_u32 s27, s18, 0
	s_add_i32 s9, s20, 0x550
	v_add_u32_e32 v4, s9, v205
	v_lshl_add_u64 v[0:1], v[0:1], 0, s[24:25]
	v_readfirstlane_b32 s9, v4
	global_load_lds_dword v[0:1], off
	s_mov_b32 m0, s9
	s_or_b32 s9, s14, 7
	s_cmpk_lt_i32 s9, 0x100
	s_cselect_b32 s18, s13, s15
	s_add_i32 s9, s18, s9
	s_mul_hi_i32 s18, s9, 0x1400
	s_mulk_i32 s9, 0x1400
	s_add_u32 s9, s52, s9
	s_addc_u32 s18, s53, s18
	v_lshl_add_u64 v[0:1], s[26:27], 0, v[2:3]
	s_add_u32 s26, s9, s80
	v_lshl_add_u64 v[0:1], v[0:1], 0, s[24:25]
	s_addc_u32 s27, s18, 0
	s_add_i32 s9, s20, 0x660
	global_load_lds_dword v[0:1], off
	v_lshl_add_u64 v[0:1], s[26:27], 0, v[2:3]
	v_add_u32_e32 v2, s9, v205
	v_lshl_add_u64 v[0:1], v[0:1], 0, s[24:25]
	v_readfirstlane_b32 s9, v2
	s_mov_b32 m0, s9
	s_movk_i32 s9, 0x480
	global_load_lds_dword v[0:1], off
	v_bfe_u32 v0, v204, 2, 2
	v_and_b32_e32 v1, 12, v204
	v_cmp_ne_u32_e32 vcc, 2, v0
	v_mov_b32_e32 v14, v3
	v_mov_b32_e32 v15, v3
	v_cndmask_b32_e32 v1, 4, v1, vcc
	v_cmp_ne_u32_e32 vcc, 1, v0
	v_mov_b32_e32 v2, v3
	v_mov_b32_e32 v4, v3
	v_cndmask_b32_e32 v0, 8, v1, vcc
	v_and_or_b32 v0, v204, 51, v0
	v_mul_lo_u32 v1, v49, s9
	v_lshlrev_b32_e32 v0, 1, v0
	v_add3_u32 v0, v205, v1, v0
	s_waitcnt vmcnt(0)
	ds_write_b16 v0, v176 offset:34816
	ds_write_b16_d16_hi v0, v176 offset:34960
	ds_write_b16 v0, v177 offset:35104
	ds_write_b16_d16_hi v0, v177 offset:35248
	ds_write_b16 v0, v178 offset:35392
	ds_write_b16_d16_hi v0, v178 offset:35536
	ds_write_b16 v0, v179 offset:35680
	ds_write_b16_d16_hi v0, v179 offset:35824
	ds_write_b16 v0, v180 offset:44032
	ds_write_b16_d16_hi v0, v180 offset:44176
	ds_write_b16 v0, v181 offset:44320
	ds_write_b16_d16_hi v0, v181 offset:44464
	ds_write_b16 v0, v182 offset:44608
	ds_write_b16_d16_hi v0, v182 offset:44752
	ds_write_b16 v0, v183 offset:44896
	ds_write_b16_d16_hi v0, v183 offset:45040
	v_mov_b32_e32 v0, v3
	v_mov_b32_e32 v1, v3
	v_mov_b32_e32 v5, v3
	v_mov_b32_e32 v6, v3
	v_mov_b32_e32 v7, v3
	v_mov_b32_e32 v8, v3
	v_mov_b32_e32 v9, v3
	v_mov_b32_e32 v10, v3
	v_mov_b32_e32 v11, v3
	v_mov_b32_e32 v12, v3
	v_mov_b32_e32 v13, v3
	v_mov_b64_e32 v[30:31], v[14:15]
	v_mov_b64_e32 v[62:63], v[14:15]
	v_mov_b64_e32 v[94:95], v[14:15]
	v_mov_b64_e32 v[126:127], v[14:15]
	v_mov_b64_e32 v[46:47], v[14:15]
	v_mov_b64_e32 v[78:79], v[14:15]
	v_mov_b64_e32 v[110:111], v[14:15]
	v_mov_b64_e32 v[142:143], v[14:15]
	s_lshl_b32 s18, s8, 5
	s_addk_i32 s21, 0xff40
	s_addk_i32 s22, 0x4040
	v_mov_b64_e32 v[28:29], v[12:13]
	v_mov_b64_e32 v[26:27], v[10:11]
	v_mov_b64_e32 v[24:25], v[8:9]
	v_mov_b64_e32 v[22:23], v[6:7]
	v_mov_b64_e32 v[20:21], v[4:5]
	v_mov_b64_e32 v[18:19], v[2:3]
	v_mov_b64_e32 v[16:17], v[0:1]
	v_mov_b64_e32 v[60:61], v[12:13]
	v_mov_b64_e32 v[58:59], v[10:11]
	v_mov_b64_e32 v[56:57], v[8:9]
	v_mov_b64_e32 v[54:55], v[6:7]
	v_mov_b64_e32 v[52:53], v[4:5]
	v_mov_b64_e32 v[50:51], v[2:3]
	v_mov_b64_e32 v[48:49], v[0:1]
	v_mov_b64_e32 v[92:93], v[12:13]
	v_mov_b64_e32 v[90:91], v[10:11]
	v_mov_b64_e32 v[88:89], v[8:9]
	v_mov_b64_e32 v[86:87], v[6:7]
	v_mov_b64_e32 v[84:85], v[4:5]
	v_mov_b64_e32 v[82:83], v[2:3]
	v_mov_b64_e32 v[80:81], v[0:1]
	v_mov_b64_e32 v[124:125], v[12:13]
	v_mov_b64_e32 v[122:123], v[10:11]
	v_mov_b64_e32 v[120:121], v[8:9]
	v_mov_b64_e32 v[118:119], v[6:7]
	v_mov_b64_e32 v[116:117], v[4:5]
	v_mov_b64_e32 v[114:115], v[2:3]
	v_mov_b64_e32 v[112:113], v[0:1]
	v_mov_b64_e32 v[44:45], v[12:13]
	v_mov_b64_e32 v[42:43], v[10:11]
	v_mov_b64_e32 v[40:41], v[8:9]
	v_mov_b64_e32 v[38:39], v[6:7]
	v_mov_b64_e32 v[36:37], v[4:5]
	v_mov_b64_e32 v[34:35], v[2:3]
	v_mov_b64_e32 v[32:33], v[0:1]
	v_mov_b64_e32 v[76:77], v[12:13]
	v_mov_b64_e32 v[74:75], v[10:11]
	v_mov_b64_e32 v[72:73], v[8:9]
	v_mov_b64_e32 v[70:71], v[6:7]
	v_mov_b64_e32 v[68:69], v[4:5]
	v_mov_b64_e32 v[66:67], v[2:3]
	v_mov_b64_e32 v[64:65], v[0:1]
	v_mov_b64_e32 v[108:109], v[12:13]
	v_mov_b64_e32 v[106:107], v[10:11]
	v_mov_b64_e32 v[104:105], v[8:9]
	v_mov_b64_e32 v[102:103], v[6:7]
	v_mov_b64_e32 v[100:101], v[4:5]
	v_mov_b64_e32 v[98:99], v[2:3]
	v_mov_b64_e32 v[96:97], v[0:1]
	v_mov_b64_e32 v[140:141], v[12:13]
	v_mov_b64_e32 v[138:139], v[10:11]
	v_mov_b64_e32 v[136:137], v[8:9]
	v_mov_b64_e32 v[134:135], v[6:7]
	v_mov_b64_e32 v[132:133], v[4:5]
	v_mov_b64_e32 v[130:131], v[2:3]
	v_mov_b64_e32 v[128:129], v[0:1]
	s_mov_b32 s26, 0
	s_waitcnt lgkmcnt(0)
	s_barrier
	v_and_b32_e32 v2, 31, v204
	v_bfe_u32 v15, v204, 5, 1
	v_lshlrev_b32_e32 v15, 4, v15
	v_or_b32_e32 v13, s18, v2
	v_mul_u32_u24_e32 v1, 0x90, v2
	v_mad_u32_u24 v0, v2, s30, v15
	v_mul_lo_u32 v13, v13, s30
	v_add_u32_e32 v0, v0, v205
	v_add3_u32 v1, v1, v15, v205
	v_add3_u32 v13, v206, v13, v15
	v_bfe_u32 v15, v204, 2, 2
	v_and_b32_e32 v2, 12, v204
	v_cmp_ne_u32_e32 vcc, 2, v15
	s_movk_i32 s8, 0x480
	v_ashrrev_i32_e32 v211, 6, v204
	v_cndmask_b32_e32 v2, 4, v2, vcc
	v_cmp_ne_u32_e32 vcc, 1, v15
	v_mul_lo_u32 v211, v211, s8
	s_nop 0
	v_cndmask_b32_e32 v15, 8, v2, vcc
	v_and_or_b32 v2, v204, 51, v15
	v_lshlrev_b32_e32 v2, 1, v2
	v_add3_u32 v2, v205, v211, v2
	v_and_b32_e32 v206, 63, v204
	v_ashrrev_i32_e32 v252, 6, v204
	s_movk_i32 s8, 0x1400
	v_lshlrev_b32_e32 v252, 4, v252
	v_mad_u32_u24 v252, v206, s8, v252
	v_lshlrev_b32_e32 v206, 2, v206
	v_add_u32_e32 v206, 0x400, v206
	s_lshr_b32 s8, s18, 5
	s_cmp_ge_u32 s8, 4
	s_cbranch_scc1 .LatB_entry

.LatB_entry:
	v_mov_b32_e32 v12, v0
	ds_read_b128 v[228:231], v12 offset:0
	ds_read_b128 v[232:235], v12 offset:32
	ds_read_b128 v[236:239], v12 offset:64
	ds_read_b128 v[240:243], v12 offset:96
	ds_read_b128 v[244:247], v13 offset:0
	ds_read_b128 v[248:251], v13 offset:32
	ds_read_b128 v[4:7], v13 offset:64
	ds_read_b128 v[8:11], v13 offset:96

.LBB0_745:
	s_and_b64 vcc, exec, s[0:1]
	s_cbranch_vccz .LBB0_454
	s_ashr_i32 s0, s22, 2
	s_lshl_b32 s15, s0, 8
	s_lshl_b32 s12, s0, 12
	s_lshl_b32 s0, s22, 7
	v_mov_b32_e32 v205, v3
	v_readlane_b32 s1, v254, 27
	s_and_b32 s8, s0, 0x180
	v_mbcnt_lo_u32_b32 v0, -1, 0
	v_mbcnt_hi_u32_b32 v0, -1, v0
	s_add_i32 s9, s15, 0x4000
	v_add_u32_e32 v204, s1, v0
	s_lshl_b32 s80, s8, 1
	s_add_u32 s0, s52, s80
	v_lshlrev_b32_e32 v0, 4, v204
	v_add_u32_e32 v6, 0x200, v204
	v_add_u32_e32 v12, 0x400, v204
	v_add_u32_e32 v14, 0x600, v204
	v_add_u32_e32 v20, 0x800, v204
	v_add_u32_e32 v22, 0xa00, v204
	v_add_u32_e32 v28, 0xc00, v204
	v_add_u32_e32 v32, 0xe00, v204
	s_addc_u32 s1, s53, 0
	v_and_b32_e32 v2, 0xf0, v0
	v_ashrrev_i32_e32 v36, 4, v204
	v_ashrrev_i32_e32 v38, 4, v6
	v_ashrrev_i32_e32 v40, 4, v12
	v_ashrrev_i32_e32 v42, 4, v14
	v_ashrrev_i32_e32 v44, 4, v20
	v_ashrrev_i32_e32 v46, 4, v22
	v_ashrrev_i32_e32 v48, 4, v28
	v_ashrrev_i32_e32 v50, 4, v32
	v_lshl_add_u64 v[0:1], s[0:1], 0, v[2:3]
	v_add_u32_e32 v4, s9, v36
	s_movk_i32 s13, 0x1400
	v_add_u32_e32 v6, s9, v38
	v_add_u32_e32 v12, s9, v40
	v_add_u32_e32 v14, s9, v42
	v_add_u32_e32 v20, s9, v44
	v_add_u32_e32 v22, s9, v46
	v_add_u32_e32 v28, s9, v48
	v_add_u32_e32 v32, s9, v50
	v_mad_i64_i32 v[4:5], s[2:3], v4, s13, v[0:1]
	v_mad_i64_i32 v[8:9], s[2:3], v6, s13, v[0:1]
	v_mad_i64_i32 v[12:13], s[2:3], v12, s13, v[0:1]
	v_mad_i64_i32 v[16:17], s[2:3], v14, s13, v[0:1]
	v_mad_i64_i32 v[20:21], s[2:3], v20, s13, v[0:1]
	v_mad_i64_i32 v[24:25], s[2:3], v22, s13, v[0:1]
	v_mad_i64_i32 v[28:29], s[2:3], v28, s13, v[0:1]
	v_mad_i64_i32 v[0:1], s[2:3], v32, s13, v[0:1]
	global_load_dwordx4 v[4:7], v[4:5], off
	s_nop 0
	global_load_dwordx4 v[8:11], v[8:9], off
	s_nop 0
	global_load_dwordx4 v[12:15], v[12:13], off
	s_nop 0
	global_load_dwordx4 v[16:19], v[16:17], off
	s_nop 0
	global_load_dwordx4 v[20:23], v[20:21], off
	s_nop 0
	global_load_dwordx4 v[24:27], v[24:25], off
	v_add_u32_e32 v206, 0x11800, v205
	global_load_dwordx4 v[28:31], v[28:29], off
	v_ashrrev_i32_e32 v51, 6, v204
	global_load_dwordx4 v[32:35], v[0:1], off
	v_add_u32_e32 v0, v206, v2
	v_mad_u64_u32 v[36:37], s[10:11], v36, s30, v[0:1]
	v_mad_u64_u32 v[38:39], s[10:11], v38, s30, v[0:1]
	v_mad_u64_u32 v[40:41], s[10:11], v40, s30, v[0:1]
	v_mad_u64_u32 v[42:43], s[10:11], v42, s30, v[0:1]
	v_mad_u64_u32 v[44:45], s[10:11], v44, s30, v[0:1]
	v_mad_u64_u32 v[46:47], s[10:11], v46, s30, v[0:1]
	v_mad_u64_u32 v[48:49], s[10:11], v48, s30, v[0:1]
	v_mad_u64_u32 v[0:1], s[10:11], v50, s30, v[0:1]
	v_and_b32_e32 v2, 63, v204
	v_readfirstlane_b32 s2, v51
	s_mov_b64 s[24:25], 0x400
	v_mov_b32_e32 v226, 0x3ecc95a3
	v_mov_b32_e32 v210, 0
	v_mov_b32_e32 v208, 0xf149f2ca
	s_waitcnt vmcnt(7)
	ds_write_b128 v36, v[4:7]
	s_waitcnt vmcnt(6)
	ds_write_b128 v38, v[8:11]
	s_waitcnt vmcnt(5)
	ds_write_b128 v40, v[12:15]
	s_waitcnt vmcnt(4)
	ds_write_b128 v42, v[16:19]
	s_waitcnt vmcnt(3)
	ds_write_b128 v44, v[20:23]
	s_waitcnt vmcnt(2)
	ds_write_b128 v46, v[24:27]
	s_waitcnt vmcnt(1)
	ds_write_b128 v48, v[28:31]
	v_or_b32_e32 v4, s9, v2
	v_lshlrev_b32_e32 v2, 2, v2
	v_mov_b32_e32 v14, v3
	s_waitcnt vmcnt(0)
	ds_write_b128 v0, v[32:35]
	v_mov_b64_e32 v[0:1], s[52:53]
	v_mad_i64_i32 v[0:1], s[10:11], v4, s13, v[0:1]
	s_lshl_b32 s10, s2, 3
	s_add_i32 s11, s12, 0xffffff00
	s_cmp_lt_i32 s2, 32
	s_cselect_b32 s3, s9, s11
	s_add_i32 s3, s3, s10
	s_mul_hi_i32 s12, s3, 0x1400
	s_mulk_i32 s3, 0x1400
	s_add_u32 s3, s52, s3
	v_lshlrev_b32_e32 v4, 3, v51
	s_addc_u32 s13, s53, s12
	v_lshl_add_u64 v[0:1], v[0:1], 0, s[80:81]
	v_ashrrev_i32_e32 v5, 31, v4
	s_add_u32 s12, s3, s80
	v_lshl_add_u64 v[0:1], v[4:5], 1, v[0:1]
	s_addc_u32 s13, s13, 0
	global_load_dwordx4 v[176:179], v[0:1], off offset:2048
	global_load_dwordx4 v[180:183], v[0:1], off offset:2176
	v_lshl_add_u64 v[0:1], s[12:13], 0, v[2:3]
	s_mul_i32 s13, s2, 0x880
	v_add_u32_e32 v4, s13, v205
	s_or_b32 s14, s10, 1
	v_readfirstlane_b32 s3, v4
	s_cmpk_lt_i32 s14, 0x100
	s_mov_b32 m0, s3
	s_cselect_b32 s3, s9, s11
	s_add_i32 s3, s3, s14
	s_mul_hi_i32 s12, s3, 0x1400
	s_mulk_i32 s3, 0x1400
	s_add_u32 s3, s52, s3
	s_mulk_i32 s14, 0x110
	s_addc_u32 s12, s53, s12
	v_add_u32_e32 v4, s14, v205
	v_lshl_add_u64 v[0:1], v[0:1], 0, s[24:25]
	s_add_u32 s22, s3, s80
	v_readfirstlane_b32 s3, v4
	global_load_lds_dword v[0:1], off
	s_addc_u32 s23, s12, 0
	s_mov_b32 m0, s3
	s_or_b32 s3, s10, 2
	s_cmpk_lt_i32 s3, 0x100
	s_cselect_b32 s12, s9, s11
	s_add_i32 s3, s12, s3
	s_mul_hi_i32 s12, s3, 0x1400
	s_mulk_i32 s3, 0x1400
	s_add_u32 s3, s52, s3
	s_addc_u32 s12, s53, s12
	v_lshl_add_u64 v[0:1], s[22:23], 0, v[2:3]
	s_add_u32 s22, s3, s80
	s_addc_u32 s23, s12, 0
	s_add_i32 s3, s14, 0x110
	v_add_u32_e32 v4, s3, v205
	v_lshl_add_u64 v[0:1], v[0:1], 0, s[24:25]
	v_readfirstlane_b32 s3, v4
	global_load_lds_dword v[0:1], off
	s_mov_b32 m0, s3
	s_or_b32 s3, s10, 3
	s_cmpk_lt_i32 s3, 0x100
	s_cselect_b32 s12, s9, s11
	s_add_i32 s3, s12, s3
	s_mul_hi_i32 s12, s3, 0x1400
	s_mulk_i32 s3, 0x1400
	s_add_u32 s3, s52, s3
	s_addc_u32 s12, s53, s12
	v_lshl_add_u64 v[0:1], s[22:23], 0, v[2:3]
	s_add_u32 s22, s3, s80
	s_addc_u32 s23, s12, 0
	s_add_i32 s3, s14, 0x220
	v_add_u32_e32 v4, s3, v205
	v_lshl_add_u64 v[0:1], v[0:1], 0, s[24:25]
	v_readfirstlane_b32 s3, v4
	global_load_lds_dword v[0:1], off
	s_mov_b32 m0, s3
	s_or_b32 s3, s10, 4
	s_cmpk_lt_i32 s3, 0x100
	s_cselect_b32 s12, s9, s11
	s_add_i32 s3, s12, s3
	s_mul_hi_i32 s12, s3, 0x1400
	s_mulk_i32 s3, 0x1400
	s_add_u32 s3, s52, s3
	s_addc_u32 s12, s53, s12
	v_lshl_add_u64 v[0:1], s[22:23], 0, v[2:3]
	s_add_u32 s22, s3, s80
	s_addc_u32 s23, s12, 0
	s_add_i32 s3, s14, 0x330
	v_add_u32_e32 v4, s3, v205
	v_lshl_add_u64 v[0:1], v[0:1], 0, s[24:25]
	v_readfirstlane_b32 s3, v4
	global_load_lds_dword v[0:1], off
	s_mov_b32 m0, s3
	s_or_b32 s3, s10, 5
	s_cmpk_lt_i32 s3, 0x100
	s_cselect_b32 s12, s9, s11
	s_add_i32 s3, s12, s3
	s_mul_hi_i32 s12, s3, 0x1400
	s_mulk_i32 s3, 0x1400
	s_add_u32 s3, s52, s3
	s_addc_u32 s12, s53, s12
	v_lshl_add_u64 v[0:1], s[22:23], 0, v[2:3]
	s_add_u32 s22, s3, s80
	s_addc_u32 s23, s12, 0
	s_add_i32 s3, s14, 0x440
	v_add_u32_e32 v4, s3, v205
	v_lshl_add_u64 v[0:1], v[0:1], 0, s[24:25]
	v_readfirstlane_b32 s3, v4
	global_load_lds_dword v[0:1], off
	s_mov_b32 m0, s3
	s_or_b32 s3, s10, 6
	s_cmpk_lt_i32 s3, 0x100
	s_cselect_b32 s12, s9, s11
	s_add_i32 s3, s12, s3
	s_mul_hi_i32 s12, s3, 0x1400
	s_mulk_i32 s3, 0x1400
	s_add_u32 s3, s52, s3
	s_addc_u32 s12, s53, s12
	v_lshl_add_u64 v[0:1], s[22:23], 0, v[2:3]
	s_add_u32 s22, s3, s80
	s_addc_u32 s23, s12, 0
	s_add_i32 s3, s14, 0x550
	v_add_u32_e32 v4, s3, v205
	v_lshl_add_u64 v[0:1], v[0:1], 0, s[24:25]
	v_readfirstlane_b32 s3, v4
	global_load_lds_dword v[0:1], off
	s_mov_b32 m0, s3
	s_or_b32 s3, s10, 7
	s_cmpk_lt_i32 s3, 0x100
	s_cselect_b32 s12, s9, s11
	s_add_i32 s3, s12, s3
	s_mul_hi_i32 s12, s3, 0x1400
	s_mulk_i32 s3, 0x1400
	s_add_u32 s3, s52, s3
	s_addc_u32 s12, s53, s12
	v_lshl_add_u64 v[0:1], s[22:23], 0, v[2:3]
	s_add_u32 s22, s3, s80
	v_lshl_add_u64 v[0:1], v[0:1], 0, s[24:25]
	s_addc_u32 s23, s12, 0
	s_add_i32 s3, s14, 0x660
	global_load_lds_dword v[0:1], off
	v_lshl_add_u64 v[0:1], s[22:23], 0, v[2:3]
	v_add_u32_e32 v2, s3, v205
	v_lshl_add_u64 v[0:1], v[0:1], 0, s[24:25]
	v_readfirstlane_b32 s3, v2
	s_mov_b32 m0, s3
	s_movk_i32 s3, 0x480
	global_load_lds_dword v[0:1], off
	v_bfe_u32 v0, v204, 2, 2
	v_and_b32_e32 v1, 12, v204
	v_cmp_ne_u32_e32 vcc, 2, v0
	v_mov_b32_e32 v15, v3
	v_mov_b32_e32 v2, v3
	v_cndmask_b32_e32 v1, 4, v1, vcc
	v_cmp_ne_u32_e32 vcc, 1, v0
	v_mov_b32_e32 v4, v3
	v_mov_b32_e32 v5, v3
	v_cndmask_b32_e32 v0, 8, v1, vcc
	v_and_or_b32 v0, v204, 51, v0
	v_mul_lo_u32 v1, v51, s3
	v_lshlrev_b32_e32 v0, 1, v0
	v_add3_u32 v0, v205, v1, v0
	s_waitcnt vmcnt(0)
	ds_write_b16 v0, v176 offset:34816
	ds_write_b16_d16_hi v0, v176 offset:34960
	ds_write_b16 v0, v177 offset:35104
	ds_write_b16_d16_hi v0, v177 offset:35248
	ds_write_b16 v0, v178 offset:35392
	ds_write_b16_d16_hi v0, v178 offset:35536
	ds_write_b16 v0, v179 offset:35680
	ds_write_b16_d16_hi v0, v179 offset:35824
	ds_write_b16 v0, v180 offset:44032
	ds_write_b16_d16_hi v0, v180 offset:44176
	ds_write_b16 v0, v181 offset:44320
	ds_write_b16_d16_hi v0, v181 offset:44464
	ds_write_b16 v0, v182 offset:44608
	ds_write_b16_d16_hi v0, v182 offset:44752
	ds_write_b16 v0, v183 offset:44896
	ds_write_b16_d16_hi v0, v183 offset:45040
	v_mov_b32_e32 v0, v3
	v_mov_b32_e32 v1, v3
	v_mov_b32_e32 v6, v3
	v_mov_b32_e32 v7, v3
	v_mov_b32_e32 v8, v3
	v_mov_b32_e32 v9, v3
	v_mov_b32_e32 v10, v3
	v_mov_b32_e32 v11, v3
	v_mov_b32_e32 v12, v3
	v_mov_b32_e32 v13, v3
	v_mov_b64_e32 v[30:31], v[14:15]
	v_mov_b64_e32 v[62:63], v[14:15]
	v_mov_b64_e32 v[94:95], v[14:15]
	v_mov_b64_e32 v[126:127], v[14:15]
	v_mov_b64_e32 v[46:47], v[14:15]
	v_mov_b64_e32 v[78:79], v[14:15]
	v_mov_b64_e32 v[110:111], v[14:15]
	v_mov_b64_e32 v[142:143], v[14:15]
	s_lshl_b32 s12, s2, 5
	s_addk_i32 s15, 0x4040
	s_mov_b32 s22, 0
	v_mov_b64_e32 v[28:29], v[12:13]
	v_mov_b64_e32 v[26:27], v[10:11]
	v_mov_b64_e32 v[24:25], v[8:9]
	v_mov_b64_e32 v[22:23], v[6:7]
	v_mov_b64_e32 v[20:21], v[4:5]
	v_mov_b64_e32 v[18:19], v[2:3]
	v_mov_b64_e32 v[16:17], v[0:1]
	v_mov_b64_e32 v[60:61], v[12:13]
	v_mov_b64_e32 v[58:59], v[10:11]
	v_mov_b64_e32 v[56:57], v[8:9]
	v_mov_b64_e32 v[54:55], v[6:7]
	v_mov_b64_e32 v[52:53], v[4:5]
	v_mov_b64_e32 v[50:51], v[2:3]
	v_mov_b64_e32 v[48:49], v[0:1]
	v_mov_b64_e32 v[92:93], v[12:13]
	v_mov_b64_e32 v[90:91], v[10:11]
	v_mov_b64_e32 v[88:89], v[8:9]
	v_mov_b64_e32 v[86:87], v[6:7]
	v_mov_b64_e32 v[84:85], v[4:5]
	v_mov_b64_e32 v[82:83], v[2:3]
	v_mov_b64_e32 v[80:81], v[0:1]
	v_mov_b64_e32 v[124:125], v[12:13]
	v_mov_b64_e32 v[122:123], v[10:11]
	v_mov_b64_e32 v[120:121], v[8:9]
	v_mov_b64_e32 v[118:119], v[6:7]
	v_mov_b64_e32 v[116:117], v[4:5]
	v_mov_b64_e32 v[114:115], v[2:3]
	v_mov_b64_e32 v[112:113], v[0:1]
	v_mov_b64_e32 v[44:45], v[12:13]
	v_mov_b64_e32 v[42:43], v[10:11]
	v_mov_b64_e32 v[40:41], v[8:9]
	v_mov_b64_e32 v[38:39], v[6:7]
	v_mov_b64_e32 v[36:37], v[4:5]
	v_mov_b64_e32 v[34:35], v[2:3]
	v_mov_b64_e32 v[32:33], v[0:1]
	v_mov_b64_e32 v[76:77], v[12:13]
	v_mov_b64_e32 v[74:75], v[10:11]
	v_mov_b64_e32 v[72:73], v[8:9]
	v_mov_b64_e32 v[70:71], v[6:7]
	v_mov_b64_e32 v[68:69], v[4:5]
	v_mov_b64_e32 v[66:67], v[2:3]
	v_mov_b64_e32 v[64:65], v[0:1]
	v_mov_b64_e32 v[108:109], v[12:13]
	v_mov_b64_e32 v[106:107], v[10:11]
	v_mov_b64_e32 v[104:105], v[8:9]
	v_mov_b64_e32 v[102:103], v[6:7]
	v_mov_b64_e32 v[100:101], v[4:5]
	v_mov_b64_e32 v[98:99], v[2:3]
	v_mov_b64_e32 v[96:97], v[0:1]
	v_mov_b64_e32 v[140:141], v[12:13]
	v_mov_b64_e32 v[138:139], v[10:11]
	v_mov_b64_e32 v[136:137], v[8:9]
	v_mov_b64_e32 v[134:135], v[6:7]
	v_mov_b64_e32 v[132:133], v[4:5]
	v_mov_b64_e32 v[130:131], v[2:3]
	v_mov_b64_e32 v[128:129], v[0:1]
	v_mov_b32_e32 v209, 0xf149f2ca
	v_mov_b32_e32 v207, 0
	s_mov_b32 s25, 0
	s_waitcnt lgkmcnt(0)
	s_barrier
	v_and_b32_e32 v2, 31, v204
	v_bfe_u32 v15, v204, 5, 1
	v_lshlrev_b32_e32 v15, 4, v15
	v_or_b32_e32 v13, s12, v2
	v_mul_u32_u24_e32 v1, 0x90, v2
	v_mad_u32_u24 v0, v2, s30, v15
	v_mul_lo_u32 v13, v13, s30
	v_add_u32_e32 v0, v0, v205
	v_add3_u32 v1, v1, v15, v205
	v_add3_u32 v13, v206, v13, v15
	v_bfe_u32 v15, v204, 2, 2
	v_and_b32_e32 v2, 12, v204
	v_cmp_ne_u32_e32 vcc, 2, v15
	s_movk_i32 s24, 0x480
	v_ashrrev_i32_e32 v211, 6, v204
	v_cndmask_b32_e32 v2, 4, v2, vcc
	v_cmp_ne_u32_e32 vcc, 1, v15
	v_mul_lo_u32 v211, v211, s24
	s_nop 0
	v_cndmask_b32_e32 v15, 8, v2, vcc
	v_and_or_b32 v2, v204, 51, v15
	v_lshlrev_b32_e32 v2, 1, v2
	v_add3_u32 v2, v205, v211, v2
	v_and_b32_e32 v206, 63, v204
	v_ashrrev_i32_e32 v252, 6, v204
	s_movk_i32 s24, 0x1400
	v_lshlrev_b32_e32 v252, 4, v252
	v_mad_u32_u24 v252, v206, s24, v252
	v_lshlrev_b32_e32 v206, 2, v206
	v_add_u32_e32 v206, 0x400, v206
	s_lshr_b32 s24, s12, 5
	s_cmp_ge_u32 s24, 4
	s_cbranch_scc1 .Lat2B_entry
